# speedup vs baseline: 1.0030x; 1.0030x over previous
.LBB2_132:
	s_load_dwordx8 s[4:11], s[0:1], 0x0
	s_load_dwordx2 s[12:13], s[0:1], 0x20
	s_load_dwordx2 s[34:35], s[0:1], 0x28
	s_lshr_b32 s24, s2, 0
	s_and_b32 s25, s2, 0
	s_mul_i32 s26, s25, 16
	s_add_u32 s27, s26, 16
	v_lshl_or_b32 v55, s24, 14, v0
	s_waitcnt lgkmcnt(0)
	s_mov_b32 s14, 0x61a80
	s_mov_b32 s15, 0xf4240
	s_mov_b32 s16, 0x155cc0
	v_mov_b32_e32 v34, s4
	v_mov_b32_e32 v37, s5
	v_mov_b32_e32 v35, s6
	v_mov_b32_e32 v38, s7
	v_mov_b32_e32 v36, s8
	v_mov_b32_e32 v39, s9
	v_mov_b32_e32 v43, 0
	v_mov_b32_e32 v47, 0
	v_mov_b32_e32 v49, 0x30d40
	v_mov_b32_e32 v50, 0xfff6d840
	v_mov_b32_e32 v48, 0x61a80
	v_mov_b32_e32 v51, 0x61a80
	v_mov_b32_e32 v52, 0xf4240
	v_mov_b32_e32 v53, 0x30d40
	v_mov_b32_e32 v54, 0x61a80
	v_cmp_gt_u32_e64 s[18:19], s14, v55
	v_cmp_gt_u32_e64 s[20:21], s15, v55
	v_cmp_gt_u32_e64 s[22:23], s16, v55
	s_nop 0
	v_cndmask_b32_e64 v44, v36, v35, s[20:21]
	v_cndmask_b32_e64 v44, v44, v34, s[18:19]
	v_cndmask_b32_e64 v45, v39, v38, s[20:21]
	v_cndmask_b32_e64 v45, v45, v37, s[18:19]
	v_cndmask_b32_e64 v42, v50, v49, s[20:21]
	v_cndmask_b32_e64 v42, v42, v48, s[18:19]
	v_add_u32_e32 v42, v42, v55
	v_cndmask_b32_e64 v42, 0, v42, s[22:23]
	v_lshl_add_u64 v[46:47], v[42:43], 2, v[44:45]
	global_load_dword v3, v[46:47], off nt
	v_cndmask_b32_e64 v42, v52, v51, s[20:21]
	v_cndmask_b32_e64 v42, v42, 0, s[18:19]
	v_sub_u32_e32 v42, v55, v42
	v_cndmask_b32_e64 v42, 0, v42, s[22:23]
	v_lshl_add_u64 v[46:47], v[42:43], 2, v[44:45]
	global_load_dword v2, v[46:47], off nt
	v_add_u32_e32 v40, 0x400, v55
	v_cmp_gt_u32_e64 s[18:19], s14, v40
	v_cmp_gt_u32_e64 s[20:21], s15, v40
	v_cmp_gt_u32_e64 s[22:23], s16, v40
	s_nop 0
	v_cndmask_b32_e64 v44, v36, v35, s[20:21]
	v_cndmask_b32_e64 v44, v44, v34, s[18:19]
	v_cndmask_b32_e64 v45, v39, v38, s[20:21]
	v_cndmask_b32_e64 v45, v45, v37, s[18:19]
	v_cndmask_b32_e64 v42, v50, v49, s[20:21]
	v_cndmask_b32_e64 v42, v42, v48, s[18:19]
	v_add_u32_e32 v42, v42, v40
	v_cndmask_b32_e64 v42, 0, v42, s[22:23]
	v_lshl_add_u64 v[46:47], v[42:43], 2, v[44:45]
	global_load_dword v5, v[46:47], off nt
	v_cndmask_b32_e64 v42, v52, v51, s[20:21]
	v_cndmask_b32_e64 v42, v42, 0, s[18:19]
	v_sub_u32_e32 v42, v40, v42
	v_cndmask_b32_e64 v42, 0, v42, s[22:23]
	v_lshl_add_u64 v[46:47], v[42:43], 2, v[44:45]
	global_load_dword v4, v[46:47], off nt
	v_add_u32_e32 v40, 0x800, v55
	v_cmp_gt_u32_e64 s[18:19], s14, v40
	v_cmp_gt_u32_e64 s[20:21], s15, v40
	v_cmp_gt_u32_e64 s[22:23], s16, v40
	s_nop 0
	v_cndmask_b32_e64 v44, v36, v35, s[20:21]
	v_cndmask_b32_e64 v44, v44, v34, s[18:19]
	v_cndmask_b32_e64 v45, v39, v38, s[20:21]
	v_cndmask_b32_e64 v45, v45, v37, s[18:19]
	v_cndmask_b32_e64 v42, v50, v49, s[20:21]
	v_cndmask_b32_e64 v42, v42, v48, s[18:19]
	v_add_u32_e32 v42, v42, v40
	v_cndmask_b32_e64 v42, 0, v42, s[22:23]
	v_lshl_add_u64 v[46:47], v[42:43], 2, v[44:45]
	global_load_dword v7, v[46:47], off nt
	v_cndmask_b32_e64 v42, v52, v51, s[20:21]
	v_cndmask_b32_e64 v42, v42, 0, s[18:19]
	v_sub_u32_e32 v42, v40, v42
	v_cndmask_b32_e64 v42, 0, v42, s[22:23]
	v_lshl_add_u64 v[46:47], v[42:43], 2, v[44:45]
	global_load_dword v6, v[46:47], off nt
	v_add_u32_e32 v40, 0xc00, v55
	v_cmp_gt_u32_e64 s[18:19], s14, v40
	v_cmp_gt_u32_e64 s[20:21], s15, v40
	v_cmp_gt_u32_e64 s[22:23], s16, v40
	s_nop 0
	v_cndmask_b32_e64 v44, v36, v35, s[20:21]
	v_cndmask_b32_e64 v44, v44, v34, s[18:19]
	v_cndmask_b32_e64 v45, v39, v38, s[20:21]
	v_cndmask_b32_e64 v45, v45, v37, s[18:19]
	v_cndmask_b32_e64 v42, v50, v49, s[20:21]
	v_cndmask_b32_e64 v42, v42, v48, s[18:19]
	v_add_u32_e32 v42, v42, v40
	v_cndmask_b32_e64 v42, 0, v42, s[22:23]
	v_lshl_add_u64 v[46:47], v[42:43], 2, v[44:45]
	global_load_dword v9, v[46:47], off nt
	v_cndmask_b32_e64 v42, v52, v51, s[20:21]
	v_cndmask_b32_e64 v42, v42, 0, s[18:19]
	v_sub_u32_e32 v42, v40, v42
	v_cndmask_b32_e64 v42, 0, v42, s[22:23]
	v_lshl_add_u64 v[46:47], v[42:43], 2, v[44:45]
	global_load_dword v8, v[46:47], off nt
	v_add_u32_e32 v40, 0x1000, v55
	v_cmp_gt_u32_e64 s[18:19], s14, v40
	v_cmp_gt_u32_e64 s[20:21], s15, v40
	v_cmp_gt_u32_e64 s[22:23], s16, v40
	s_nop 0
	v_cndmask_b32_e64 v44, v36, v35, s[20:21]
	v_cndmask_b32_e64 v44, v44, v34, s[18:19]
	v_cndmask_b32_e64 v45, v39, v38, s[20:21]
	v_cndmask_b32_e64 v45, v45, v37, s[18:19]
	v_cndmask_b32_e64 v42, v50, v49, s[20:21]
	v_cndmask_b32_e64 v42, v42, v48, s[18:19]
	v_add_u32_e32 v42, v42, v40
	v_cndmask_b32_e64 v42, 0, v42, s[22:23]
	v_lshl_add_u64 v[46:47], v[42:43], 2, v[44:45]
	global_load_dword v11, v[46:47], off nt
	v_cndmask_b32_e64 v42, v52, v51, s[20:21]
	v_cndmask_b32_e64 v42, v42, 0, s[18:19]
	v_sub_u32_e32 v42, v40, v42
	v_cndmask_b32_e64 v42, 0, v42, s[22:23]
	v_lshl_add_u64 v[46:47], v[42:43], 2, v[44:45]
	global_load_dword v10, v[46:47], off nt
	v_add_u32_e32 v40, 0x1400, v55
	v_cmp_gt_u32_e64 s[18:19], s14, v40
	v_cmp_gt_u32_e64 s[20:21], s15, v40
	v_cmp_gt_u32_e64 s[22:23], s16, v40
	s_nop 0
	v_cndmask_b32_e64 v44, v36, v35, s[20:21]
	v_cndmask_b32_e64 v44, v44, v34, s[18:19]
	v_cndmask_b32_e64 v45, v39, v38, s[20:21]
	v_cndmask_b32_e64 v45, v45, v37, s[18:19]
	v_cndmask_b32_e64 v42, v50, v49, s[20:21]
	v_cndmask_b32_e64 v42, v42, v48, s[18:19]
	v_add_u32_e32 v42, v42, v40
	v_cndmask_b32_e64 v42, 0, v42, s[22:23]
	v_lshl_add_u64 v[46:47], v[42:43], 2, v[44:45]
	global_load_dword v13, v[46:47], off nt
	v_cndmask_b32_e64 v42, v52, v51, s[20:21]
	v_cndmask_b32_e64 v42, v42, 0, s[18:19]
	v_sub_u32_e32 v42, v40, v42
	v_cndmask_b32_e64 v42, 0, v42, s[22:23]
	v_lshl_add_u64 v[46:47], v[42:43], 2, v[44:45]
	global_load_dword v12, v[46:47], off nt
	v_add_u32_e32 v40, 0x1800, v55
	v_cmp_gt_u32_e64 s[18:19], s14, v40
	v_cmp_gt_u32_e64 s[20:21], s15, v40
	v_cmp_gt_u32_e64 s[22:23], s16, v40
	s_nop 0
	v_cndmask_b32_e64 v44, v36, v35, s[20:21]
	v_cndmask_b32_e64 v44, v44, v34, s[18:19]
	v_cndmask_b32_e64 v45, v39, v38, s[20:21]
	v_cndmask_b32_e64 v45, v45, v37, s[18:19]
	v_cndmask_b32_e64 v42, v50, v49, s[20:21]
	v_cndmask_b32_e64 v42, v42, v48, s[18:19]
	v_add_u32_e32 v42, v42, v40
	v_cndmask_b32_e64 v42, 0, v42, s[22:23]
	v_lshl_add_u64 v[46:47], v[42:43], 2, v[44:45]
	global_load_dword v15, v[46:47], off nt
	v_cndmask_b32_e64 v42, v52, v51, s[20:21]
	v_cndmask_b32_e64 v42, v42, 0, s[18:19]
	v_sub_u32_e32 v42, v40, v42
	v_cndmask_b32_e64 v42, 0, v42, s[22:23]
	v_lshl_add_u64 v[46:47], v[42:43], 2, v[44:45]
	global_load_dword v14, v[46:47], off nt
	v_add_u32_e32 v40, 0x1c00, v55
	v_cmp_gt_u32_e64 s[18:19], s14, v40
	v_cmp_gt_u32_e64 s[20:21], s15, v40
	v_cmp_gt_u32_e64 s[22:23], s16, v40
	s_nop 0
	v_cndmask_b32_e64 v44, v36, v35, s[20:21]
	v_cndmask_b32_e64 v44, v44, v34, s[18:19]
	v_cndmask_b32_e64 v45, v39, v38, s[20:21]
	v_cndmask_b32_e64 v45, v45, v37, s[18:19]
	v_cndmask_b32_e64 v42, v50, v49, s[20:21]
	v_cndmask_b32_e64 v42, v42, v48, s[18:19]
	v_add_u32_e32 v42, v42, v40
	v_cndmask_b32_e64 v42, 0, v42, s[22:23]
	v_lshl_add_u64 v[46:47], v[42:43], 2, v[44:45]
	global_load_dword v17, v[46:47], off nt
	v_cndmask_b32_e64 v42, v52, v51, s[20:21]
	v_cndmask_b32_e64 v42, v42, 0, s[18:19]
	v_sub_u32_e32 v42, v40, v42
	v_cndmask_b32_e64 v42, 0, v42, s[22:23]
	v_lshl_add_u64 v[46:47], v[42:43], 2, v[44:45]
	global_load_dword v16, v[46:47], off nt
	v_add_u32_e32 v40, 0x2000, v55
	v_cmp_gt_u32_e64 s[18:19], s14, v40
	v_cmp_gt_u32_e64 s[20:21], s15, v40
	v_cmp_gt_u32_e64 s[22:23], s16, v40
	s_nop 0
	v_cndmask_b32_e64 v44, v36, v35, s[20:21]
	v_cndmask_b32_e64 v44, v44, v34, s[18:19]
	v_cndmask_b32_e64 v45, v39, v38, s[20:21]
	v_cndmask_b32_e64 v45, v45, v37, s[18:19]
	v_cndmask_b32_e64 v42, v50, v49, s[20:21]
	v_cndmask_b32_e64 v42, v42, v48, s[18:19]
	v_add_u32_e32 v42, v42, v40
	v_cndmask_b32_e64 v42, 0, v42, s[22:23]
	v_lshl_add_u64 v[46:47], v[42:43], 2, v[44:45]
	global_load_dword v19, v[46:47], off nt
	v_cndmask_b32_e64 v42, v52, v51, s[20:21]
	v_cndmask_b32_e64 v42, v42, 0, s[18:19]
	v_sub_u32_e32 v42, v40, v42
	v_cndmask_b32_e64 v42, 0, v42, s[22:23]
	v_lshl_add_u64 v[46:47], v[42:43], 2, v[44:45]
	global_load_dword v18, v[46:47], off nt
	v_add_u32_e32 v40, 0x2400, v55
	v_cmp_gt_u32_e64 s[18:19], s14, v40
	v_cmp_gt_u32_e64 s[20:21], s15, v40
	v_cmp_gt_u32_e64 s[22:23], s16, v40
	s_nop 0
	v_cndmask_b32_e64 v44, v36, v35, s[20:21]
	v_cndmask_b32_e64 v44, v44, v34, s[18:19]
	v_cndmask_b32_e64 v45, v39, v38, s[20:21]
	v_cndmask_b32_e64 v45, v45, v37, s[18:19]
	v_cndmask_b32_e64 v42, v50, v49, s[20:21]
	v_cndmask_b32_e64 v42, v42, v48, s[18:19]
	v_add_u32_e32 v42, v42, v40
	v_cndmask_b32_e64 v42, 0, v42, s[22:23]
	v_lshl_add_u64 v[46:47], v[42:43], 2, v[44:45]
	global_load_dword v21, v[46:47], off nt
	v_cndmask_b32_e64 v42, v52, v51, s[20:21]
	v_cndmask_b32_e64 v42, v42, 0, s[18:19]
	v_sub_u32_e32 v42, v40, v42
	v_cndmask_b32_e64 v42, 0, v42, s[22:23]
	v_lshl_add_u64 v[46:47], v[42:43], 2, v[44:45]
	global_load_dword v20, v[46:47], off nt
	v_add_u32_e32 v40, 0x2800, v55
	v_cmp_gt_u32_e64 s[18:19], s14, v40
	v_cmp_gt_u32_e64 s[20:21], s15, v40
	v_cmp_gt_u32_e64 s[22:23], s16, v40
	s_nop 0
	v_cndmask_b32_e64 v44, v36, v35, s[20:21]
	v_cndmask_b32_e64 v44, v44, v34, s[18:19]
	v_cndmask_b32_e64 v45, v39, v38, s[20:21]
	v_cndmask_b32_e64 v45, v45, v37, s[18:19]
	v_cndmask_b32_e64 v42, v50, v49, s[20:21]
	v_cndmask_b32_e64 v42, v42, v48, s[18:19]
	v_add_u32_e32 v42, v42, v40
	v_cndmask_b32_e64 v42, 0, v42, s[22:23]
	v_lshl_add_u64 v[46:47], v[42:43], 2, v[44:45]
	global_load_dword v23, v[46:47], off nt
	v_cndmask_b32_e64 v42, v52, v51, s[20:21]
	v_cndmask_b32_e64 v42, v42, 0, s[18:19]
	v_sub_u32_e32 v42, v40, v42
	v_cndmask_b32_e64 v42, 0, v42, s[22:23]
	v_lshl_add_u64 v[46:47], v[42:43], 2, v[44:45]
	global_load_dword v22, v[46:47], off nt
	v_add_u32_e32 v40, 0x2c00, v55
	v_cmp_gt_u32_e64 s[18:19], s14, v40
	v_cmp_gt_u32_e64 s[20:21], s15, v40
	v_cmp_gt_u32_e64 s[22:23], s16, v40
	s_nop 0
	v_cndmask_b32_e64 v44, v36, v35, s[20:21]
	v_cndmask_b32_e64 v44, v44, v34, s[18:19]
	v_cndmask_b32_e64 v45, v39, v38, s[20:21]
	v_cndmask_b32_e64 v45, v45, v37, s[18:19]
	v_cndmask_b32_e64 v42, v50, v49, s[20:21]
	v_cndmask_b32_e64 v42, v42, v48, s[18:19]
	v_add_u32_e32 v42, v42, v40
	v_cndmask_b32_e64 v42, 0, v42, s[22:23]
	v_lshl_add_u64 v[46:47], v[42:43], 2, v[44:45]
	global_load_dword v25, v[46:47], off nt
	v_cndmask_b32_e64 v42, v52, v51, s[20:21]
	v_cndmask_b32_e64 v42, v42, 0, s[18:19]
	v_sub_u32_e32 v42, v40, v42
	v_cndmask_b32_e64 v42, 0, v42, s[22:23]
	v_lshl_add_u64 v[46:47], v[42:43], 2, v[44:45]
	global_load_dword v24, v[46:47], off nt
	v_add_u32_e32 v40, 0x3000, v55
	v_cmp_gt_u32_e64 s[18:19], s14, v40
	v_cmp_gt_u32_e64 s[20:21], s15, v40
	v_cmp_gt_u32_e64 s[22:23], s16, v40
	s_nop 0
	v_cndmask_b32_e64 v44, v36, v35, s[20:21]
	v_cndmask_b32_e64 v44, v44, v34, s[18:19]
	v_cndmask_b32_e64 v45, v39, v38, s[20:21]
	v_cndmask_b32_e64 v45, v45, v37, s[18:19]
	v_cndmask_b32_e64 v42, v50, v49, s[20:21]
	v_cndmask_b32_e64 v42, v42, v48, s[18:19]
	v_add_u32_e32 v42, v42, v40
	v_cndmask_b32_e64 v42, 0, v42, s[22:23]
	v_lshl_add_u64 v[46:47], v[42:43], 2, v[44:45]
	global_load_dword v27, v[46:47], off nt
	v_cndmask_b32_e64 v42, v52, v51, s[20:21]
	v_cndmask_b32_e64 v42, v42, 0, s[18:19]
	v_sub_u32_e32 v42, v40, v42
	v_cndmask_b32_e64 v42, 0, v42, s[22:23]
	v_lshl_add_u64 v[46:47], v[42:43], 2, v[44:45]
	global_load_dword v26, v[46:47], off nt
	v_add_u32_e32 v40, 0x3400, v55
	v_cmp_gt_u32_e64 s[18:19], s14, v40
	v_cmp_gt_u32_e64 s[20:21], s15, v40
	v_cmp_gt_u32_e64 s[22:23], s16, v40
	s_nop 0
	v_cndmask_b32_e64 v44, v36, v35, s[20:21]
	v_cndmask_b32_e64 v44, v44, v34, s[18:19]
	v_cndmask_b32_e64 v45, v39, v38, s[20:21]
	v_cndmask_b32_e64 v45, v45, v37, s[18:19]
	v_cndmask_b32_e64 v42, v50, v49, s[20:21]
	v_cndmask_b32_e64 v42, v42, v48, s[18:19]
	v_add_u32_e32 v42, v42, v40
	v_cndmask_b32_e64 v42, 0, v42, s[22:23]
	v_lshl_add_u64 v[46:47], v[42:43], 2, v[44:45]
	global_load_dword v29, v[46:47], off nt
	v_cndmask_b32_e64 v42, v52, v51, s[20:21]
	v_cndmask_b32_e64 v42, v42, 0, s[18:19]
	v_sub_u32_e32 v42, v40, v42
	v_cndmask_b32_e64 v42, 0, v42, s[22:23]
	v_lshl_add_u64 v[46:47], v[42:43], 2, v[44:45]
	global_load_dword v28, v[46:47], off nt
	v_add_u32_e32 v40, 0x3800, v55
	v_cmp_gt_u32_e64 s[18:19], s14, v40
	v_cmp_gt_u32_e64 s[20:21], s15, v40
	v_cmp_gt_u32_e64 s[22:23], s16, v40
	s_nop 0
	v_cndmask_b32_e64 v44, v36, v35, s[20:21]
	v_cndmask_b32_e64 v44, v44, v34, s[18:19]
	v_cndmask_b32_e64 v45, v39, v38, s[20:21]
	v_cndmask_b32_e64 v45, v45, v37, s[18:19]
	v_cndmask_b32_e64 v42, v50, v49, s[20:21]
	v_cndmask_b32_e64 v42, v42, v48, s[18:19]
	v_add_u32_e32 v42, v42, v40
	v_cndmask_b32_e64 v42, 0, v42, s[22:23]
	v_lshl_add_u64 v[46:47], v[42:43], 2, v[44:45]
	global_load_dword v31, v[46:47], off nt
	v_cndmask_b32_e64 v42, v52, v51, s[20:21]
	v_cndmask_b32_e64 v42, v42, 0, s[18:19]
	v_sub_u32_e32 v42, v40, v42
	v_cndmask_b32_e64 v42, 0, v42, s[22:23]
	v_lshl_add_u64 v[46:47], v[42:43], 2, v[44:45]
	global_load_dword v30, v[46:47], off nt
	v_add_u32_e32 v40, 0x3c00, v55
	v_cmp_gt_u32_e64 s[18:19], s14, v40
	v_cmp_gt_u32_e64 s[20:21], s15, v40
	v_cmp_gt_u32_e64 s[22:23], s16, v40
	s_nop 0
	v_cndmask_b32_e64 v44, v36, v35, s[20:21]
	v_cndmask_b32_e64 v44, v44, v34, s[18:19]
	v_cndmask_b32_e64 v45, v39, v38, s[20:21]
	v_cndmask_b32_e64 v45, v45, v37, s[18:19]
	v_cndmask_b32_e64 v42, v50, v49, s[20:21]
	v_cndmask_b32_e64 v42, v42, v48, s[18:19]
	v_add_u32_e32 v42, v42, v40
	v_cndmask_b32_e64 v42, 0, v42, s[22:23]
	v_lshl_add_u64 v[46:47], v[42:43], 2, v[44:45]
	global_load_dword v33, v[46:47], off nt
	v_cndmask_b32_e64 v42, v52, v51, s[20:21]
	v_cndmask_b32_e64 v42, v42, 0, s[18:19]
	v_sub_u32_e32 v42, v40, v42
	v_cndmask_b32_e64 v42, 0, v42, s[22:23]
	v_lshl_add_u64 v[46:47], v[42:43], 2, v[44:45]
	global_load_dword v32, v[46:47], off nt
	v_mov_b32_e32 v34, 0
	v_mov_b32_e32 v35, 0
	v_mov_b32_e32 v36, 0
	v_mov_b32_e32 v37, 0
	v_lshlrev_b32_e32 v38, 3, v0
	v_cmp_gt_u32_e32 vcc, 0x224, v0
	s_and_saveexec_b64 s[36:37], vcc
	s_cbranch_execz .Lsc_nohist
	global_load_dwordx2 v[40:41], v38, s[10:11]
	v_add_u32_e32 v39, 0x1120, v38
	global_load_dwordx2 v[42:43], v39, s[10:11]
	v_add_u32_e32 v39, 0x2240, v38
	global_load_dwordx2 v[44:45], v39, s[10:11]
	v_add_u32_e32 v39, 0x3360, v38
	global_load_dwordx2 v[46:47], v39, s[10:11]
	v_add_u32_e32 v39, 0x4480, v38
	global_load_dwordx2 v[48:49], v39, s[10:11]
	v_add_u32_e32 v39, 0x55a0, v38
	global_load_dwordx2 v[50:51], v39, s[10:11]
	v_add_u32_e32 v39, 0x66c0, v38
	global_load_dwordx2 v[52:53], v39, s[10:11]
	v_add_u32_e32 v39, 0x77e0, v38
	global_load_dwordx2 v[54:55], v39, s[10:11]
	v_add_u32_e32 v39, 0x8900, v38
	global_load_dwordx2 v[56:57], v39, s[10:11]
	v_add_u32_e32 v39, 0x9a20, v38
	global_load_dwordx2 v[58:59], v39, s[10:11]
	v_add_u32_e32 v39, 0xab40, v38
	global_load_dwordx2 v[60:61], v39, s[10:11]
	v_add_u32_e32 v39, 0xbc60, v38
	global_load_dwordx2 v[62:63], v39, s[10:11]
	v_add_u32_e32 v39, 0xcd80, v38
	global_load_dwordx2 v[64:65], v39, s[10:11]
	v_add_u32_e32 v39, 0xdea0, v38
	global_load_dwordx2 v[66:67], v39, s[10:11]
	v_add_u32_e32 v39, 0xefc0, v38
	global_load_dwordx2 v[68:69], v39, s[10:11]
	v_add_u32_e32 v39, 0x100e0, v38
	global_load_dwordx2 v[70:71], v39, s[10:11]
	v_add_u32_e32 v39, 0x11200, v38
	global_load_dwordx2 v[72:73], v39, s[10:11]
	v_add_u32_e32 v39, 0x12320, v38
	global_load_dwordx2 v[74:75], v39, s[10:11]
	v_add_u32_e32 v39, 0x13440, v38
	global_load_dwordx2 v[76:77], v39, s[10:11]
	v_add_u32_e32 v39, 0x14560, v38
	global_load_dwordx2 v[78:79], v39, s[10:11]
	v_add_u32_e32 v39, 0x15680, v38
	global_load_dwordx2 v[80:81], v39, s[10:11]
	v_add_u32_e32 v39, 0x167a0, v38
	global_load_dwordx2 v[82:83], v39, s[10:11]
	v_add_u32_e32 v39, 0x178c0, v38
	global_load_dwordx2 v[84:85], v39, s[10:11]
	v_add_u32_e32 v39, 0x189e0, v38
	global_load_dwordx2 v[86:87], v39, s[10:11]
	s_waitcnt vmcnt(23)
	s_cmp_gt_u32 s24, 0
	s_cselect_b32 s3, 1, 0
	v_add_u32_e32 v34, v34, v40
	v_add_u32_e32 v35, v35, v41
	v_mad_u32_u24 v36, v40, s3, v36
	v_mad_u32_u24 v37, v41, s3, v37
	v_add_u32_e32 v39, 0x19b00, v38
	global_load_dwordx2 v[40:41], v39, s[10:11]
	s_waitcnt vmcnt(23)
	s_cmp_gt_u32 s24, 1
	s_cselect_b32 s3, 1, 0
	v_add_u32_e32 v34, v34, v42
	v_add_u32_e32 v35, v35, v43
	v_mad_u32_u24 v36, v42, s3, v36
	v_mad_u32_u24 v37, v43, s3, v37
	v_add_u32_e32 v39, 0x1ac20, v38
	global_load_dwordx2 v[42:43], v39, s[10:11]
	s_waitcnt vmcnt(23)
	s_cmp_gt_u32 s24, 2
	s_cselect_b32 s3, 1, 0
	v_add_u32_e32 v34, v34, v44
	v_add_u32_e32 v35, v35, v45
	v_mad_u32_u24 v36, v44, s3, v36
	v_mad_u32_u24 v37, v45, s3, v37
	v_add_u32_e32 v39, 0x1bd40, v38
	global_load_dwordx2 v[44:45], v39, s[10:11]
	s_waitcnt vmcnt(23)
	s_cmp_gt_u32 s24, 3
	s_cselect_b32 s3, 1, 0
	v_add_u32_e32 v34, v34, v46
	v_add_u32_e32 v35, v35, v47
	v_mad_u32_u24 v36, v46, s3, v36
	v_mad_u32_u24 v37, v47, s3, v37
	v_add_u32_e32 v39, 0x1ce60, v38
	global_load_dwordx2 v[46:47], v39, s[10:11]
	s_waitcnt vmcnt(23)
	s_cmp_gt_u32 s24, 4
	s_cselect_b32 s3, 1, 0
	v_add_u32_e32 v34, v34, v48
	v_add_u32_e32 v35, v35, v49
	v_mad_u32_u24 v36, v48, s3, v36
	v_mad_u32_u24 v37, v49, s3, v37
	v_add_u32_e32 v39, 0x1df80, v38
	global_load_dwordx2 v[48:49], v39, s[10:11]
	s_waitcnt vmcnt(23)
	s_cmp_gt_u32 s24, 5
	s_cselect_b32 s3, 1, 0
	v_add_u32_e32 v34, v34, v50
	v_add_u32_e32 v35, v35, v51
	v_mad_u32_u24 v36, v50, s3, v36
	v_mad_u32_u24 v37, v51, s3, v37
	v_add_u32_e32 v39, 0x1f0a0, v38
	global_load_dwordx2 v[50:51], v39, s[10:11]
	s_waitcnt vmcnt(23)
	s_cmp_gt_u32 s24, 6
	s_cselect_b32 s3, 1, 0
	v_add_u32_e32 v34, v34, v52
	v_add_u32_e32 v35, v35, v53
	v_mad_u32_u24 v36, v52, s3, v36
	v_mad_u32_u24 v37, v53, s3, v37
	v_add_u32_e32 v39, 0x201c0, v38
	global_load_dwordx2 v[52:53], v39, s[10:11]
	s_waitcnt vmcnt(23)
	s_cmp_gt_u32 s24, 7
	s_cselect_b32 s3, 1, 0
	v_add_u32_e32 v34, v34, v54
	v_add_u32_e32 v35, v35, v55
	v_mad_u32_u24 v36, v54, s3, v36
	v_mad_u32_u24 v37, v55, s3, v37
	v_add_u32_e32 v39, 0x212e0, v38
	global_load_dwordx2 v[54:55], v39, s[10:11]
	s_waitcnt vmcnt(23)
	s_cmp_gt_u32 s24, 8
	s_cselect_b32 s3, 1, 0
	v_add_u32_e32 v34, v34, v56
	v_add_u32_e32 v35, v35, v57
	v_mad_u32_u24 v36, v56, s3, v36
	v_mad_u32_u24 v37, v57, s3, v37
	v_add_u32_e32 v39, 0x22400, v38
	global_load_dwordx2 v[56:57], v39, s[10:11]
	s_waitcnt vmcnt(23)
	s_cmp_gt_u32 s24, 9
	s_cselect_b32 s3, 1, 0
	v_add_u32_e32 v34, v34, v58
	v_add_u32_e32 v35, v35, v59
	v_mad_u32_u24 v36, v58, s3, v36
	v_mad_u32_u24 v37, v59, s3, v37
	v_add_u32_e32 v39, 0x23520, v38
	global_load_dwordx2 v[58:59], v39, s[10:11]
	s_waitcnt vmcnt(23)
	s_cmp_gt_u32 s24, 10
	s_cselect_b32 s3, 1, 0
	v_add_u32_e32 v34, v34, v60
	v_add_u32_e32 v35, v35, v61
	v_mad_u32_u24 v36, v60, s3, v36
	v_mad_u32_u24 v37, v61, s3, v37
	v_add_u32_e32 v39, 0x24640, v38
	global_load_dwordx2 v[60:61], v39, s[10:11]
	s_waitcnt vmcnt(23)
	s_cmp_gt_u32 s24, 11
	s_cselect_b32 s3, 1, 0
	v_add_u32_e32 v34, v34, v62
	v_add_u32_e32 v35, v35, v63
	v_mad_u32_u24 v36, v62, s3, v36
	v_mad_u32_u24 v37, v63, s3, v37
	v_add_u32_e32 v39, 0x25760, v38
	global_load_dwordx2 v[62:63], v39, s[10:11]
	s_waitcnt vmcnt(23)
	s_cmp_gt_u32 s24, 12
	s_cselect_b32 s3, 1, 0
	v_add_u32_e32 v34, v34, v64
	v_add_u32_e32 v35, v35, v65
	v_mad_u32_u24 v36, v64, s3, v36
	v_mad_u32_u24 v37, v65, s3, v37
	v_add_u32_e32 v39, 0x26880, v38
	global_load_dwordx2 v[64:65], v39, s[10:11]
	s_waitcnt vmcnt(23)
	s_cmp_gt_u32 s24, 13
	s_cselect_b32 s3, 1, 0
	v_add_u32_e32 v34, v34, v66
	v_add_u32_e32 v35, v35, v67
	v_mad_u32_u24 v36, v66, s3, v36
	v_mad_u32_u24 v37, v67, s3, v37
	v_add_u32_e32 v39, 0x279a0, v38
	global_load_dwordx2 v[66:67], v39, s[10:11]
	s_waitcnt vmcnt(23)
	s_cmp_gt_u32 s24, 14
	s_cselect_b32 s3, 1, 0
	v_add_u32_e32 v34, v34, v68
	v_add_u32_e32 v35, v35, v69
	v_mad_u32_u24 v36, v68, s3, v36
	v_mad_u32_u24 v37, v69, s3, v37
	v_add_u32_e32 v39, 0x28ac0, v38
	global_load_dwordx2 v[68:69], v39, s[10:11]
	s_waitcnt vmcnt(23)
	s_cmp_gt_u32 s24, 15
	s_cselect_b32 s3, 1, 0
	v_add_u32_e32 v34, v34, v70
	v_add_u32_e32 v35, v35, v71
	v_mad_u32_u24 v36, v70, s3, v36
	v_mad_u32_u24 v37, v71, s3, v37
	v_add_u32_e32 v39, 0x29be0, v38
	global_load_dwordx2 v[70:71], v39, s[10:11]
	s_waitcnt vmcnt(23)
	s_cmp_gt_u32 s24, 16
	s_cselect_b32 s3, 1, 0
	v_add_u32_e32 v34, v34, v72
	v_add_u32_e32 v35, v35, v73
	v_mad_u32_u24 v36, v72, s3, v36
	v_mad_u32_u24 v37, v73, s3, v37
	v_add_u32_e32 v39, 0x2ad00, v38
	global_load_dwordx2 v[72:73], v39, s[10:11]
	s_waitcnt vmcnt(23)
	s_cmp_gt_u32 s24, 17
	s_cselect_b32 s3, 1, 0
	v_add_u32_e32 v34, v34, v74
	v_add_u32_e32 v35, v35, v75
	v_mad_u32_u24 v36, v74, s3, v36
	v_mad_u32_u24 v37, v75, s3, v37
	v_add_u32_e32 v39, 0x2be20, v38
	global_load_dwordx2 v[74:75], v39, s[10:11]
	s_waitcnt vmcnt(23)
	s_cmp_gt_u32 s24, 18
	s_cselect_b32 s3, 1, 0
	v_add_u32_e32 v34, v34, v76
	v_add_u32_e32 v35, v35, v77
	v_mad_u32_u24 v36, v76, s3, v36
	v_mad_u32_u24 v37, v77, s3, v37
	v_add_u32_e32 v39, 0x2cf40, v38
	global_load_dwordx2 v[76:77], v39, s[10:11]
	s_waitcnt vmcnt(23)
	s_cmp_gt_u32 s24, 19
	s_cselect_b32 s3, 1, 0
	v_add_u32_e32 v34, v34, v78
	v_add_u32_e32 v35, v35, v79
	v_mad_u32_u24 v36, v78, s3, v36
	v_mad_u32_u24 v37, v79, s3, v37
	v_add_u32_e32 v39, 0x2e060, v38
	global_load_dwordx2 v[78:79], v39, s[10:11]
	s_waitcnt vmcnt(23)
	s_cmp_gt_u32 s24, 20
	s_cselect_b32 s3, 1, 0
	v_add_u32_e32 v34, v34, v80
	v_add_u32_e32 v35, v35, v81
	v_mad_u32_u24 v36, v80, s3, v36
	v_mad_u32_u24 v37, v81, s3, v37
	v_add_u32_e32 v39, 0x2f180, v38
	global_load_dwordx2 v[80:81], v39, s[10:11]
	s_waitcnt vmcnt(23)
	s_cmp_gt_u32 s24, 21
	s_cselect_b32 s3, 1, 0
	v_add_u32_e32 v34, v34, v82
	v_add_u32_e32 v35, v35, v83
	v_mad_u32_u24 v36, v82, s3, v36
	v_mad_u32_u24 v37, v83, s3, v37
	v_add_u32_e32 v39, 0x302a0, v38
	global_load_dwordx2 v[82:83], v39, s[10:11]
	s_waitcnt vmcnt(23)
	s_cmp_gt_u32 s24, 22
	s_cselect_b32 s3, 1, 0
	v_add_u32_e32 v34, v34, v84
	v_add_u32_e32 v35, v35, v85
	v_mad_u32_u24 v36, v84, s3, v36
	v_mad_u32_u24 v37, v85, s3, v37
	v_add_u32_e32 v39, 0x313c0, v38
	global_load_dwordx2 v[84:85], v39, s[10:11]
	s_waitcnt vmcnt(23)
	s_cmp_gt_u32 s24, 23
	s_cselect_b32 s3, 1, 0
	v_add_u32_e32 v34, v34, v86
	v_add_u32_e32 v35, v35, v87
	v_mad_u32_u24 v36, v86, s3, v36
	v_mad_u32_u24 v37, v87, s3, v37
	v_add_u32_e32 v39, 0x324e0, v38
	global_load_dwordx2 v[86:87], v39, s[10:11]
	s_waitcnt vmcnt(23)
	s_cmp_gt_u32 s24, 24
	s_cselect_b32 s3, 1, 0
	v_add_u32_e32 v34, v34, v40
	v_add_u32_e32 v35, v35, v41
	v_mad_u32_u24 v36, v40, s3, v36
	v_mad_u32_u24 v37, v41, s3, v37
	v_add_u32_e32 v39, 0x33600, v38
	global_load_dwordx2 v[40:41], v39, s[10:11]
	s_waitcnt vmcnt(23)
	s_cmp_gt_u32 s24, 25
	s_cselect_b32 s3, 1, 0
	v_add_u32_e32 v34, v34, v42
	v_add_u32_e32 v35, v35, v43
	v_mad_u32_u24 v36, v42, s3, v36
	v_mad_u32_u24 v37, v43, s3, v37
	v_add_u32_e32 v39, 0x34720, v38
	global_load_dwordx2 v[42:43], v39, s[10:11]
	s_waitcnt vmcnt(23)
	s_cmp_gt_u32 s24, 26
	s_cselect_b32 s3, 1, 0
	v_add_u32_e32 v34, v34, v44
	v_add_u32_e32 v35, v35, v45
	v_mad_u32_u24 v36, v44, s3, v36
	v_mad_u32_u24 v37, v45, s3, v37
	v_add_u32_e32 v39, 0x35840, v38
	global_load_dwordx2 v[44:45], v39, s[10:11]
	s_waitcnt vmcnt(23)
	s_cmp_gt_u32 s24, 27
	s_cselect_b32 s3, 1, 0
	v_add_u32_e32 v34, v34, v46
	v_add_u32_e32 v35, v35, v47
	v_mad_u32_u24 v36, v46, s3, v36
	v_mad_u32_u24 v37, v47, s3, v37
	v_add_u32_e32 v39, 0x36960, v38
	global_load_dwordx2 v[46:47], v39, s[10:11]
	s_waitcnt vmcnt(23)
	s_cmp_gt_u32 s24, 28
	s_cselect_b32 s3, 1, 0
	v_add_u32_e32 v34, v34, v48
	v_add_u32_e32 v35, v35, v49
	v_mad_u32_u24 v36, v48, s3, v36
	v_mad_u32_u24 v37, v49, s3, v37
	v_add_u32_e32 v39, 0x37a80, v38
	global_load_dwordx2 v[48:49], v39, s[10:11]
	s_waitcnt vmcnt(23)
	s_cmp_gt_u32 s24, 29
	s_cselect_b32 s3, 1, 0
	v_add_u32_e32 v34, v34, v50
	v_add_u32_e32 v35, v35, v51
	v_mad_u32_u24 v36, v50, s3, v36
	v_mad_u32_u24 v37, v51, s3, v37
	v_add_u32_e32 v39, 0x38ba0, v38
	global_load_dwordx2 v[50:51], v39, s[10:11]
	s_waitcnt vmcnt(23)
	s_cmp_gt_u32 s24, 30
	s_cselect_b32 s3, 1, 0
	v_add_u32_e32 v34, v34, v52
	v_add_u32_e32 v35, v35, v53
	v_mad_u32_u24 v36, v52, s3, v36
	v_mad_u32_u24 v37, v53, s3, v37
	v_add_u32_e32 v39, 0x39cc0, v38
	global_load_dwordx2 v[52:53], v39, s[10:11]
	s_waitcnt vmcnt(23)
	s_cmp_gt_u32 s24, 31
	s_cselect_b32 s3, 1, 0
	v_add_u32_e32 v34, v34, v54
	v_add_u32_e32 v35, v35, v55
	v_mad_u32_u24 v36, v54, s3, v36
	v_mad_u32_u24 v37, v55, s3, v37
	v_add_u32_e32 v39, 0x3ade0, v38
	global_load_dwordx2 v[54:55], v39, s[10:11]
	s_waitcnt vmcnt(23)
	s_cmp_gt_u32 s24, 32
	s_cselect_b32 s3, 1, 0
	v_add_u32_e32 v34, v34, v56
	v_add_u32_e32 v35, v35, v57
	v_mad_u32_u24 v36, v56, s3, v36
	v_mad_u32_u24 v37, v57, s3, v37
	v_add_u32_e32 v39, 0x3bf00, v38
	global_load_dwordx2 v[56:57], v39, s[10:11]
	s_waitcnt vmcnt(23)
	s_cmp_gt_u32 s24, 33
	s_cselect_b32 s3, 1, 0
	v_add_u32_e32 v34, v34, v58
	v_add_u32_e32 v35, v35, v59
	v_mad_u32_u24 v36, v58, s3, v36
	v_mad_u32_u24 v37, v59, s3, v37
	v_add_u32_e32 v39, 0x3d020, v38
	global_load_dwordx2 v[58:59], v39, s[10:11]
	s_waitcnt vmcnt(23)
	s_cmp_gt_u32 s24, 34
	s_cselect_b32 s3, 1, 0
	v_add_u32_e32 v34, v34, v60
	v_add_u32_e32 v35, v35, v61
	v_mad_u32_u24 v36, v60, s3, v36
	v_mad_u32_u24 v37, v61, s3, v37
	v_add_u32_e32 v39, 0x3e140, v38
	global_load_dwordx2 v[60:61], v39, s[10:11]
	s_waitcnt vmcnt(23)
	s_cmp_gt_u32 s24, 35
	s_cselect_b32 s3, 1, 0
	v_add_u32_e32 v34, v34, v62
	v_add_u32_e32 v35, v35, v63
	v_mad_u32_u24 v36, v62, s3, v36
	v_mad_u32_u24 v37, v63, s3, v37
	v_add_u32_e32 v39, 0x3f260, v38
	global_load_dwordx2 v[62:63], v39, s[10:11]
	s_waitcnt vmcnt(23)
	s_cmp_gt_u32 s24, 36
	s_cselect_b32 s3, 1, 0
	v_add_u32_e32 v34, v34, v64
	v_add_u32_e32 v35, v35, v65
	v_mad_u32_u24 v36, v64, s3, v36
	v_mad_u32_u24 v37, v65, s3, v37
	v_add_u32_e32 v39, 0x40380, v38
	global_load_dwordx2 v[64:65], v39, s[10:11]
	s_waitcnt vmcnt(23)
	s_cmp_gt_u32 s24, 37
	s_cselect_b32 s3, 1, 0
	v_add_u32_e32 v34, v34, v66
	v_add_u32_e32 v35, v35, v67
	v_mad_u32_u24 v36, v66, s3, v36
	v_mad_u32_u24 v37, v67, s3, v37
	v_add_u32_e32 v39, 0x414a0, v38
	global_load_dwordx2 v[66:67], v39, s[10:11]
	s_waitcnt vmcnt(23)
	s_cmp_gt_u32 s24, 38
	s_cselect_b32 s3, 1, 0
	v_add_u32_e32 v34, v34, v68
	v_add_u32_e32 v35, v35, v69
	v_mad_u32_u24 v36, v68, s3, v36
	v_mad_u32_u24 v37, v69, s3, v37
	v_add_u32_e32 v39, 0x425c0, v38
	global_load_dwordx2 v[68:69], v39, s[10:11]
	s_waitcnt vmcnt(23)
	s_cmp_gt_u32 s24, 39
	s_cselect_b32 s3, 1, 0
	v_add_u32_e32 v34, v34, v70
	v_add_u32_e32 v35, v35, v71
	v_mad_u32_u24 v36, v70, s3, v36
	v_mad_u32_u24 v37, v71, s3, v37
	v_add_u32_e32 v39, 0x436e0, v38
	global_load_dwordx2 v[70:71], v39, s[10:11]
	s_waitcnt vmcnt(23)
	s_cmp_gt_u32 s24, 40
	s_cselect_b32 s3, 1, 0
	v_add_u32_e32 v34, v34, v72
	v_add_u32_e32 v35, v35, v73
	v_mad_u32_u24 v36, v72, s3, v36
	v_mad_u32_u24 v37, v73, s3, v37
	v_add_u32_e32 v39, 0x44800, v38
	global_load_dwordx2 v[72:73], v39, s[10:11]
	s_waitcnt vmcnt(23)
	s_cmp_gt_u32 s24, 41
	s_cselect_b32 s3, 1, 0
	v_add_u32_e32 v34, v34, v74
	v_add_u32_e32 v35, v35, v75
	v_mad_u32_u24 v36, v74, s3, v36
	v_mad_u32_u24 v37, v75, s3, v37
	v_add_u32_e32 v39, 0x45920, v38
	global_load_dwordx2 v[74:75], v39, s[10:11]
	s_waitcnt vmcnt(23)
	s_cmp_gt_u32 s24, 42
	s_cselect_b32 s3, 1, 0
	v_add_u32_e32 v34, v34, v76
	v_add_u32_e32 v35, v35, v77
	v_mad_u32_u24 v36, v76, s3, v36
	v_mad_u32_u24 v37, v77, s3, v37
	v_add_u32_e32 v39, 0x46a40, v38
	global_load_dwordx2 v[76:77], v39, s[10:11]
	s_waitcnt vmcnt(23)
	s_cmp_gt_u32 s24, 43
	s_cselect_b32 s3, 1, 0
	v_add_u32_e32 v34, v34, v78
	v_add_u32_e32 v35, v35, v79
	v_mad_u32_u24 v36, v78, s3, v36
	v_mad_u32_u24 v37, v79, s3, v37
	v_add_u32_e32 v39, 0x47b60, v38
	global_load_dwordx2 v[78:79], v39, s[10:11]
	s_waitcnt vmcnt(23)
	s_cmp_gt_u32 s24, 44
	s_cselect_b32 s3, 1, 0
	v_add_u32_e32 v34, v34, v80
	v_add_u32_e32 v35, v35, v81
	v_mad_u32_u24 v36, v80, s3, v36
	v_mad_u32_u24 v37, v81, s3, v37
	v_add_u32_e32 v39, 0x48c80, v38
	global_load_dwordx2 v[80:81], v39, s[10:11]
	s_waitcnt vmcnt(23)
	s_cmp_gt_u32 s24, 45
	s_cselect_b32 s3, 1, 0
	v_add_u32_e32 v34, v34, v82
	v_add_u32_e32 v35, v35, v83
	v_mad_u32_u24 v36, v82, s3, v36
	v_mad_u32_u24 v37, v83, s3, v37
	v_add_u32_e32 v39, 0x49da0, v38
	global_load_dwordx2 v[82:83], v39, s[10:11]
	s_waitcnt vmcnt(23)
	s_cmp_gt_u32 s24, 46
	s_cselect_b32 s3, 1, 0
	v_add_u32_e32 v34, v34, v84
	v_add_u32_e32 v35, v35, v85
	v_mad_u32_u24 v36, v84, s3, v36
	v_mad_u32_u24 v37, v85, s3, v37
	v_add_u32_e32 v39, 0x4aec0, v38
	global_load_dwordx2 v[84:85], v39, s[10:11]
	s_waitcnt vmcnt(23)
	s_cmp_gt_u32 s24, 47
	s_cselect_b32 s3, 1, 0
	v_add_u32_e32 v34, v34, v86
	v_add_u32_e32 v35, v35, v87
	v_mad_u32_u24 v36, v86, s3, v36
	v_mad_u32_u24 v37, v87, s3, v37
	v_add_u32_e32 v39, 0x4bfe0, v38
	global_load_dwordx2 v[86:87], v39, s[10:11]
	s_waitcnt vmcnt(23)
	s_cmp_gt_u32 s24, 48
	s_cselect_b32 s3, 1, 0
	v_add_u32_e32 v34, v34, v40
	v_add_u32_e32 v35, v35, v41
	v_mad_u32_u24 v36, v40, s3, v36
	v_mad_u32_u24 v37, v41, s3, v37
	v_add_u32_e32 v39, 0x4d100, v38
	global_load_dwordx2 v[40:41], v39, s[10:11]
	s_waitcnt vmcnt(23)
	s_cmp_gt_u32 s24, 49
	s_cselect_b32 s3, 1, 0
	v_add_u32_e32 v34, v34, v42
	v_add_u32_e32 v35, v35, v43
	v_mad_u32_u24 v36, v42, s3, v36
	v_mad_u32_u24 v37, v43, s3, v37
	v_add_u32_e32 v39, 0x4e220, v38
	global_load_dwordx2 v[42:43], v39, s[10:11]
	s_waitcnt vmcnt(23)
	s_cmp_gt_u32 s24, 50
	s_cselect_b32 s3, 1, 0
	v_add_u32_e32 v34, v34, v44
	v_add_u32_e32 v35, v35, v45
	v_mad_u32_u24 v36, v44, s3, v36
	v_mad_u32_u24 v37, v45, s3, v37
	v_add_u32_e32 v39, 0x4f340, v38
	global_load_dwordx2 v[44:45], v39, s[10:11]
	s_waitcnt vmcnt(23)
	s_cmp_gt_u32 s24, 51
	s_cselect_b32 s3, 1, 0
	v_add_u32_e32 v34, v34, v46
	v_add_u32_e32 v35, v35, v47
	v_mad_u32_u24 v36, v46, s3, v36
	v_mad_u32_u24 v37, v47, s3, v37
	v_add_u32_e32 v39, 0x50460, v38
	global_load_dwordx2 v[46:47], v39, s[10:11]
	s_waitcnt vmcnt(23)
	s_cmp_gt_u32 s24, 52
	s_cselect_b32 s3, 1, 0
	v_add_u32_e32 v34, v34, v48
	v_add_u32_e32 v35, v35, v49
	v_mad_u32_u24 v36, v48, s3, v36
	v_mad_u32_u24 v37, v49, s3, v37
	v_add_u32_e32 v39, 0x51580, v38
	global_load_dwordx2 v[48:49], v39, s[10:11]
	s_waitcnt vmcnt(23)
	s_cmp_gt_u32 s24, 53
	s_cselect_b32 s3, 1, 0
	v_add_u32_e32 v34, v34, v50
	v_add_u32_e32 v35, v35, v51
	v_mad_u32_u24 v36, v50, s3, v36
	v_mad_u32_u24 v37, v51, s3, v37
	v_add_u32_e32 v39, 0x526a0, v38
	global_load_dwordx2 v[50:51], v39, s[10:11]
	s_waitcnt vmcnt(23)
	s_cmp_gt_u32 s24, 54
	s_cselect_b32 s3, 1, 0
	v_add_u32_e32 v34, v34, v52
	v_add_u32_e32 v35, v35, v53
	v_mad_u32_u24 v36, v52, s3, v36
	v_mad_u32_u24 v37, v53, s3, v37
	v_add_u32_e32 v39, 0x537c0, v38
	global_load_dwordx2 v[52:53], v39, s[10:11]
	s_waitcnt vmcnt(23)
	s_cmp_gt_u32 s24, 55
	s_cselect_b32 s3, 1, 0
	v_add_u32_e32 v34, v34, v54
	v_add_u32_e32 v35, v35, v55
	v_mad_u32_u24 v36, v54, s3, v36
	v_mad_u32_u24 v37, v55, s3, v37
	v_add_u32_e32 v39, 0x548e0, v38
	global_load_dwordx2 v[54:55], v39, s[10:11]
	s_waitcnt vmcnt(23)
	s_cmp_gt_u32 s24, 56
	s_cselect_b32 s3, 1, 0
	v_add_u32_e32 v34, v34, v56
	v_add_u32_e32 v35, v35, v57
	v_mad_u32_u24 v36, v56, s3, v36
	v_mad_u32_u24 v37, v57, s3, v37
	v_add_u32_e32 v39, 0x55a00, v38
	global_load_dwordx2 v[56:57], v39, s[10:11]
	s_waitcnt vmcnt(23)
	s_cmp_gt_u32 s24, 57
	s_cselect_b32 s3, 1, 0
	v_add_u32_e32 v34, v34, v58
	v_add_u32_e32 v35, v35, v59
	v_mad_u32_u24 v36, v58, s3, v36
	v_mad_u32_u24 v37, v59, s3, v37
	v_add_u32_e32 v39, 0x56b20, v38
	global_load_dwordx2 v[58:59], v39, s[10:11]
	s_waitcnt vmcnt(23)
	s_cmp_gt_u32 s24, 58
	s_cselect_b32 s3, 1, 0
	v_add_u32_e32 v34, v34, v60
	v_add_u32_e32 v35, v35, v61
	v_mad_u32_u24 v36, v60, s3, v36
	v_mad_u32_u24 v37, v61, s3, v37
	v_add_u32_e32 v39, 0x57c40, v38
	global_load_dwordx2 v[60:61], v39, s[10:11]
	s_waitcnt vmcnt(23)
	s_cmp_gt_u32 s24, 59
	s_cselect_b32 s3, 1, 0
	v_add_u32_e32 v34, v34, v62
	v_add_u32_e32 v35, v35, v63
	v_mad_u32_u24 v36, v62, s3, v36
	v_mad_u32_u24 v37, v63, s3, v37
	v_add_u32_e32 v39, 0x58d60, v38
	global_load_dwordx2 v[62:63], v39, s[10:11]
	s_waitcnt vmcnt(23)
	s_cmp_gt_u32 s24, 60
	s_cselect_b32 s3, 1, 0
	v_add_u32_e32 v34, v34, v64
	v_add_u32_e32 v35, v35, v65
	v_mad_u32_u24 v36, v64, s3, v36
	v_mad_u32_u24 v37, v65, s3, v37
	v_add_u32_e32 v39, 0x59e80, v38
	global_load_dwordx2 v[64:65], v39, s[10:11]
	s_waitcnt vmcnt(23)
	s_cmp_gt_u32 s24, 61
	s_cselect_b32 s3, 1, 0
	v_add_u32_e32 v34, v34, v66
	v_add_u32_e32 v35, v35, v67
	v_mad_u32_u24 v36, v66, s3, v36
	v_mad_u32_u24 v37, v67, s3, v37
	v_add_u32_e32 v39, 0x5afa0, v38
	global_load_dwordx2 v[66:67], v39, s[10:11]
	s_waitcnt vmcnt(23)
	s_cmp_gt_u32 s24, 62
	s_cselect_b32 s3, 1, 0
	v_add_u32_e32 v34, v34, v68
	v_add_u32_e32 v35, v35, v69
	v_mad_u32_u24 v36, v68, s3, v36
	v_mad_u32_u24 v37, v69, s3, v37
	s_waitcnt vmcnt(22)
	s_cmp_gt_u32 s24, 63
	s_cselect_b32 s3, 1, 0
	v_add_u32_e32 v34, v34, v70
	v_add_u32_e32 v35, v35, v71
	v_mad_u32_u24 v36, v70, s3, v36
	v_mad_u32_u24 v37, v71, s3, v37
	s_waitcnt vmcnt(21)
	s_cmp_gt_u32 s24, 64
	s_cselect_b32 s3, 1, 0
	v_add_u32_e32 v34, v34, v72
	v_add_u32_e32 v35, v35, v73
	v_mad_u32_u24 v36, v72, s3, v36
	v_mad_u32_u24 v37, v73, s3, v37
	s_waitcnt vmcnt(20)
	s_cmp_gt_u32 s24, 65
	s_cselect_b32 s3, 1, 0
	v_add_u32_e32 v34, v34, v74
	v_add_u32_e32 v35, v35, v75
	v_mad_u32_u24 v36, v74, s3, v36
	v_mad_u32_u24 v37, v75, s3, v37
	s_waitcnt vmcnt(19)
	s_cmp_gt_u32 s24, 66
	s_cselect_b32 s3, 1, 0
	v_add_u32_e32 v34, v34, v76
	v_add_u32_e32 v35, v35, v77
	v_mad_u32_u24 v36, v76, s3, v36
	v_mad_u32_u24 v37, v77, s3, v37
	s_waitcnt vmcnt(18)
	s_cmp_gt_u32 s24, 67
	s_cselect_b32 s3, 1, 0
	v_add_u32_e32 v34, v34, v78
	v_add_u32_e32 v35, v35, v79
	v_mad_u32_u24 v36, v78, s3, v36
	v_mad_u32_u24 v37, v79, s3, v37
	s_waitcnt vmcnt(17)
	s_cmp_gt_u32 s24, 68
	s_cselect_b32 s3, 1, 0
	v_add_u32_e32 v34, v34, v80
	v_add_u32_e32 v35, v35, v81
	v_mad_u32_u24 v36, v80, s3, v36
	v_mad_u32_u24 v37, v81, s3, v37
	s_waitcnt vmcnt(16)
	s_cmp_gt_u32 s24, 69
	s_cselect_b32 s3, 1, 0
	v_add_u32_e32 v34, v34, v82
	v_add_u32_e32 v35, v35, v83
	v_mad_u32_u24 v36, v82, s3, v36
	v_mad_u32_u24 v37, v83, s3, v37
	s_waitcnt vmcnt(15)
	s_cmp_gt_u32 s24, 70
	s_cselect_b32 s3, 1, 0
	v_add_u32_e32 v34, v34, v84
	v_add_u32_e32 v35, v35, v85
	v_mad_u32_u24 v36, v84, s3, v36
	v_mad_u32_u24 v37, v85, s3, v37
	s_waitcnt vmcnt(14)
	s_cmp_gt_u32 s24, 71
	s_cselect_b32 s3, 1, 0
	v_add_u32_e32 v34, v34, v86
	v_add_u32_e32 v35, v35, v87
	v_mad_u32_u24 v36, v86, s3, v36
	v_mad_u32_u24 v37, v87, s3, v37
	s_waitcnt vmcnt(13)
	s_cmp_gt_u32 s24, 72
	s_cselect_b32 s3, 1, 0
	v_add_u32_e32 v34, v34, v40
	v_add_u32_e32 v35, v35, v41
	v_mad_u32_u24 v36, v40, s3, v36
	v_mad_u32_u24 v37, v41, s3, v37
	s_waitcnt vmcnt(12)
	s_cmp_gt_u32 s24, 73
	s_cselect_b32 s3, 1, 0
	v_add_u32_e32 v34, v34, v42
	v_add_u32_e32 v35, v35, v43
	v_mad_u32_u24 v36, v42, s3, v36
	v_mad_u32_u24 v37, v43, s3, v37
	s_waitcnt vmcnt(11)
	s_cmp_gt_u32 s24, 74
	s_cselect_b32 s3, 1, 0
	v_add_u32_e32 v34, v34, v44
	v_add_u32_e32 v35, v35, v45
	v_mad_u32_u24 v36, v44, s3, v36
	v_mad_u32_u24 v37, v45, s3, v37
	s_waitcnt vmcnt(10)
	s_cmp_gt_u32 s24, 75
	s_cselect_b32 s3, 1, 0
	v_add_u32_e32 v34, v34, v46
	v_add_u32_e32 v35, v35, v47
	v_mad_u32_u24 v36, v46, s3, v36
	v_mad_u32_u24 v37, v47, s3, v37
	s_waitcnt vmcnt(9)
	s_cmp_gt_u32 s24, 76
	s_cselect_b32 s3, 1, 0
	v_add_u32_e32 v34, v34, v48
	v_add_u32_e32 v35, v35, v49
	v_mad_u32_u24 v36, v48, s3, v36
	v_mad_u32_u24 v37, v49, s3, v37
	s_waitcnt vmcnt(8)
	s_cmp_gt_u32 s24, 77
	s_cselect_b32 s3, 1, 0
	v_add_u32_e32 v34, v34, v50
	v_add_u32_e32 v35, v35, v51
	v_mad_u32_u24 v36, v50, s3, v36
	v_mad_u32_u24 v37, v51, s3, v37
	s_waitcnt vmcnt(7)
	s_cmp_gt_u32 s24, 78
	s_cselect_b32 s3, 1, 0
	v_add_u32_e32 v34, v34, v52
	v_add_u32_e32 v35, v35, v53
	v_mad_u32_u24 v36, v52, s3, v36
	v_mad_u32_u24 v37, v53, s3, v37
	s_waitcnt vmcnt(6)
	s_cmp_gt_u32 s24, 79
	s_cselect_b32 s3, 1, 0
	v_add_u32_e32 v34, v34, v54
	v_add_u32_e32 v35, v35, v55
	v_mad_u32_u24 v36, v54, s3, v36
	v_mad_u32_u24 v37, v55, s3, v37
	s_waitcnt vmcnt(5)
	s_cmp_gt_u32 s24, 80
	s_cselect_b32 s3, 1, 0
	v_add_u32_e32 v34, v34, v56
	v_add_u32_e32 v35, v35, v57
	v_mad_u32_u24 v36, v56, s3, v36
	v_mad_u32_u24 v37, v57, s3, v37
	s_waitcnt vmcnt(4)
	s_cmp_gt_u32 s24, 81
	s_cselect_b32 s3, 1, 0
	v_add_u32_e32 v34, v34, v58
	v_add_u32_e32 v35, v35, v59
	v_mad_u32_u24 v36, v58, s3, v36
	v_mad_u32_u24 v37, v59, s3, v37
	s_waitcnt vmcnt(3)
	s_cmp_gt_u32 s24, 82
	s_cselect_b32 s3, 1, 0
	v_add_u32_e32 v34, v34, v60
	v_add_u32_e32 v35, v35, v61
	v_mad_u32_u24 v36, v60, s3, v36
	v_mad_u32_u24 v37, v61, s3, v37
	s_waitcnt vmcnt(2)
	s_cmp_gt_u32 s24, 83
	s_cselect_b32 s3, 1, 0
	v_add_u32_e32 v34, v34, v62
	v_add_u32_e32 v35, v35, v63
	v_mad_u32_u24 v36, v62, s3, v36
	v_mad_u32_u24 v37, v63, s3, v37
	s_waitcnt vmcnt(1)
	s_cmp_gt_u32 s24, 84
	s_cselect_b32 s3, 1, 0
	v_add_u32_e32 v34, v34, v64
	v_add_u32_e32 v35, v35, v65
	v_mad_u32_u24 v36, v64, s3, v36
	v_mad_u32_u24 v37, v65, s3, v37
	s_waitcnt vmcnt(0)
	s_cmp_gt_u32 s24, 85
	s_cselect_b32 s3, 1, 0
	v_add_u32_e32 v34, v34, v66
	v_add_u32_e32 v35, v35, v67
	v_mad_u32_u24 v36, v66, s3, v36
	v_mad_u32_u24 v37, v67, s3, v37
